# v47 + diff-attention unit epilogue: the 16 row-sum cross-lane reductions (16x5 ds_bpermute) batched per step instead of an 80-step serial bpermute->wait->add ladder
# baseline (speedup 1.0000x reference)
.LBB0_224:
	s_or_b64 exec, exec, s[0:1]
	v_ashrrev_i32_e32 v14, 5, v0
	s_xor_b32 s44, s13, 0x80000000
	s_mov_b32 s0, s44
	v_lshl_add_u32 v147, v14, 4, s6
	s_waitcnt lgkmcnt(0)
	ds_read_b128 v[6:9], v147
	ds_read_b128 v[2:5], v147 offset:32
	ds_read_b128 v[148:151], v147 offset:128
	v_mov_b32_e32 v144, v112
	v_mov_b32_e32 v145, v128
	s_waitcnt lgkmcnt(0)
	v_rcp_f32_e32 v10, v6
	v_mov_b32_e32 v152, v48
	v_rcp_f32_e32 v6, v148
	v_mov_b32_e32 v153, v16
	v_mov_b32_e32 v128, v113
	v_mov_b32_e32 v16, v49
	v_mul_f32_e32 v11, s0, v6
	v_pk_mul_f32 v[144:145], v[144:145], v[10:11]
	v_rcp_f32_e32 v6, v7
	v_rcp_f32_e32 v7, v149
	v_add_f32_e32 v112, v144, v145
	v_mov_b32_e32 v144, v96
	v_mov_b32_e32 v145, v80
	v_pk_mul_f32 v[144:145], v[144:145], v[10:11]
	v_mul_f32_e32 v7, s0, v7
	v_add_f32_e32 v96, v144, v145
	v_mov_b32_e32 v144, v64
	v_mov_b32_e32 v145, v32
	v_pk_mul_f32 v[144:145], v[144:145], v[10:11]
	v_pk_mul_f32 v[10:11], v[152:153], v[10:11]
	v_add_f32_e32 v144, v144, v145
	v_add_f32_e32 v145, v10, v11
	v_pk_mul_f32 v[10:11], v[128:129], v[6:7]
	v_mov_b32_e32 v80, v97
	v_add_f32_e32 v48, v10, v11
	v_pk_mul_f32 v[10:11], v[80:81], v[6:7]
	v_mov_b32_e32 v32, v65
	v_add_f32_e32 v64, v10, v11
	v_pk_mul_f32 v[10:11], v[32:33], v[6:7]
	v_pk_mul_f32 v[6:7], v[16:17], v[6:7]
	v_add_f32_e32 v33, v10, v11
	v_add_f32_e32 v49, v6, v7
	v_rcp_f32_e32 v7, v150
	v_rcp_f32_e32 v6, v8
	v_mov_b32_e32 v10, v114
	v_mov_b32_e32 v11, v130
	v_mul_f32_e32 v7, s0, v7
	v_pk_mul_f32 v[10:11], v[10:11], v[6:7]
	v_mov_b32_e32 v130, v115
	v_add_f32_e32 v15, v10, v11
	v_mov_b32_e32 v10, v98
	v_mov_b32_e32 v11, v82
	v_pk_mul_f32 v[10:11], v[10:11], v[6:7]
	v_mov_b32_e32 v82, v99
	v_add_f32_e32 v17, v10, v11
	v_mov_b32_e32 v10, v66
	v_mov_b32_e32 v11, v34
	v_pk_mul_f32 v[10:11], v[10:11], v[6:7]
	v_mov_b32_e32 v34, v67
	v_add_f32_e32 v65, v10, v11
	v_mov_b32_e32 v10, v50
	v_mov_b32_e32 v11, v18
	v_pk_mul_f32 v[6:7], v[10:11], v[6:7]
	v_mov_b32_e32 v18, v51
	v_add_f32_e32 v50, v6, v7
	v_rcp_f32_e32 v7, v151
	v_rcp_f32_e32 v6, v9
	v_rcp_f32_e32 v10, v2
	v_mov_b32_e32 v66, v116
	v_mul_f32_e32 v7, s0, v7
	v_pk_mul_f32 v[8:9], v[130:131], v[6:7]
	v_mov_b32_e32 v67, v132
	v_add_f32_e32 v16, v8, v9
	v_pk_mul_f32 v[8:9], v[82:83], v[6:7]
	v_mov_b32_e32 v132, v117
	v_add_f32_e32 v32, v8, v9
	v_pk_mul_f32 v[8:9], v[34:35], v[6:7]
	v_pk_mul_f32 v[6:7], v[18:19], v[6:7]
	v_add_f32_e32 v34, v8, v9
	v_add_f32_e32 v18, v6, v7
	ds_read_b128 v[6:9], v147 offset:160
	v_mov_b32_e32 v82, v72
	v_mov_b32_e32 v83, v40
	v_mov_b32_e32 v40, v73
	v_mul_f32_e32 v146, v112, v112
	s_waitcnt lgkmcnt(0)
	v_rcp_f32_e32 v2, v6
	v_fmac_f32_e32 v146, v96, v96
	v_fmac_f32_e32 v146, v144, v144
	v_fmac_f32_e32 v146, v145, v145
	v_mul_f32_e32 v11, s0, v2
	v_pk_mul_f32 v[66:67], v[66:67], v[10:11]
	v_rcp_f32_e32 v2, v3
	v_rcp_f32_e32 v3, v7
	v_add_f32_e32 v19, v66, v67
	v_mov_b32_e32 v66, v100
	v_mov_b32_e32 v67, v84
	v_pk_mul_f32 v[66:67], v[66:67], v[10:11]
	v_mul_f32_e32 v3, s0, v3
	v_add_f32_e32 v35, v66, v67
	v_mov_b32_e32 v66, v68
	v_mov_b32_e32 v67, v36
	v_pk_mul_f32 v[66:67], v[66:67], v[10:11]
	v_pk_mul_f32 v[6:7], v[132:133], v[2:3]
	v_add_f32_e32 v51, v66, v67
	v_mov_b32_e32 v66, v52
	v_mov_b32_e32 v67, v20
	v_mov_b32_e32 v84, v101
	v_pk_mul_f32 v[10:11], v[66:67], v[10:11]
	v_add_f32_e32 v66, v6, v7
	v_pk_mul_f32 v[6:7], v[84:85], v[2:3]
	v_mov_b32_e32 v36, v69
	v_mov_b32_e32 v20, v53
	v_add_f32_e32 v67, v6, v7
	v_pk_mul_f32 v[6:7], v[36:37], v[2:3]
	v_pk_mul_f32 v[2:3], v[20:21], v[2:3]
	v_add_f32_e32 v36, v6, v7
	v_add_f32_e32 v20, v2, v3
	v_rcp_f32_e32 v3, v8
	v_rcp_f32_e32 v2, v4
	v_mov_b32_e32 v6, v118
	v_mov_b32_e32 v7, v134
	v_mul_f32_e32 v3, s0, v3
	v_pk_mul_f32 v[6:7], v[6:7], v[2:3]
	v_mov_b32_e32 v134, v119
	v_add_f32_e32 v21, v6, v7
	v_mov_b32_e32 v6, v102
	v_mov_b32_e32 v7, v86
	v_pk_mul_f32 v[6:7], v[6:7], v[2:3]
	v_mov_b32_e32 v86, v103
	v_add_f32_e32 v37, v6, v7
	v_mov_b32_e32 v6, v70
	v_mov_b32_e32 v7, v38
	v_pk_mul_f32 v[6:7], v[6:7], v[2:3]
	v_mov_b32_e32 v38, v71
	v_add_f32_e32 v53, v6, v7
	v_mov_b32_e32 v6, v54
	v_mov_b32_e32 v7, v22
	v_pk_mul_f32 v[2:3], v[6:7], v[2:3]
	v_mov_b32_e32 v22, v55
	v_add_f32_e32 v54, v2, v3
	v_rcp_f32_e32 v3, v9
	v_rcp_f32_e32 v2, v5
	ds_read_b128 v[6:9], v147 offset:192
	v_add_f32_e32 v52, v10, v11
	v_mul_f32_e32 v3, s0, v3
	v_pk_mul_f32 v[4:5], v[134:135], v[2:3]
	v_mov_b32_e32 v70, v120
	v_add_f32_e32 v68, v4, v5
	v_pk_mul_f32 v[4:5], v[86:87], v[2:3]
	v_mov_b32_e32 v71, v136
	v_add_f32_e32 v69, v4, v5
	v_pk_mul_f32 v[4:5], v[38:39], v[2:3]
	v_pk_mul_f32 v[2:3], v[22:23], v[2:3]
	v_add_f32_e32 v38, v4, v5
	v_add_f32_e32 v22, v2, v3
	ds_read_b128 v[2:5], v147 offset:64
	v_mov_b32_e32 v136, v121
	v_mul_f32_e32 v113, v48, v48
	v_fmac_f32_e32 v113, v64, v64
	v_fmac_f32_e32 v113, v33, v33
	s_waitcnt lgkmcnt(0)
	v_rcp_f32_e32 v10, v2
	v_rcp_f32_e32 v2, v6
	v_fmac_f32_e32 v113, v49, v49
	v_mul_f32_e32 v97, v15, v15
	v_fmac_f32_e32 v97, v17, v17
	v_mul_f32_e32 v11, s0, v2
	v_rcp_f32_e32 v2, v3
	v_rcp_f32_e32 v3, v7
	v_pk_mul_f32 v[70:71], v[70:71], v[10:11]
	v_pk_mul_f32 v[82:83], v[82:83], v[10:11]
	v_add_f32_e32 v39, v70, v71
	v_mul_f32_e32 v3, s0, v3
	v_mov_b32_e32 v71, v88
	v_pk_mul_f32 v[6:7], v[136:137], v[2:3]
	v_mov_b32_e32 v88, v105
	v_add_f32_e32 v72, v82, v83
	v_mov_b32_e32 v83, v24
	v_add_f32_e32 v55, v6, v7
	v_pk_mul_f32 v[6:7], v[88:89], v[2:3]
	v_mov_b32_e32 v24, v57
	v_mov_b32_e32 v82, v56
	v_add_f32_e32 v56, v6, v7
	v_pk_mul_f32 v[6:7], v[40:41], v[2:3]
	v_pk_mul_f32 v[2:3], v[24:25], v[2:3]
	v_add_f32_e32 v41, v6, v7
	v_add_f32_e32 v57, v2, v3
	v_rcp_f32_e32 v3, v8
	v_rcp_f32_e32 v2, v4
	v_mov_b32_e32 v6, v122
	v_mov_b32_e32 v7, v138
	v_mul_f32_e32 v3, s0, v3
	v_pk_mul_f32 v[6:7], v[6:7], v[2:3]
	v_mov_b32_e32 v70, v104
	v_add_f32_e32 v23, v6, v7
	v_mov_b32_e32 v6, v106
	v_mov_b32_e32 v7, v90
	v_pk_mul_f32 v[6:7], v[6:7], v[2:3]
	v_pk_mul_f32 v[70:71], v[70:71], v[10:11]
	v_add_f32_e32 v25, v6, v7
	v_mov_b32_e32 v6, v74
	v_mov_b32_e32 v7, v42
	v_pk_mul_f32 v[6:7], v[6:7], v[2:3]
	v_add_f32_e32 v70, v70, v71
	v_add_f32_e32 v71, v6, v7
	v_mov_b32_e32 v6, v58
	v_mov_b32_e32 v7, v26
	v_pk_mul_f32 v[2:3], v[6:7], v[2:3]
	v_mov_b32_e32 v138, v123
	v_add_f32_e32 v58, v2, v3
	v_rcp_f32_e32 v3, v9
	v_rcp_f32_e32 v2, v5
	v_mov_b32_e32 v90, v107
	v_mov_b32_e32 v42, v75
	v_mul_f32_e32 v3, s0, v3
	v_pk_mul_f32 v[4:5], v[138:139], v[2:3]
	v_mov_b32_e32 v26, v59
	v_add_f32_e32 v24, v4, v5
	v_pk_mul_f32 v[4:5], v[90:91], v[2:3]
	ds_read_b128 v[6:9], v147 offset:224
	v_add_f32_e32 v40, v4, v5
	v_pk_mul_f32 v[4:5], v[42:43], v[2:3]
	v_pk_mul_f32 v[2:3], v[26:27], v[2:3]
	v_add_f32_e32 v42, v4, v5
	v_add_f32_e32 v26, v2, v3
	ds_read_b128 v[2:5], v147 offset:96
	v_pk_mul_f32 v[10:11], v[82:83], v[10:11]
	v_mov_b32_e32 v74, v124
	v_add_f32_e32 v80, v10, v11
	v_mov_b32_e32 v75, v140
	s_waitcnt lgkmcnt(0)
	v_rcp_f32_e32 v10, v2
	v_rcp_f32_e32 v2, v6
	v_rcp_f32_e32 v86, v3
	v_rcp_f32_e32 v3, v7
	v_mov_b32_e32 v140, v125
	v_mul_f32_e32 v11, s0, v2
	v_pk_mul_f32 v[74:75], v[74:75], v[10:11]
	v_mul_f32_e32 v87, s0, v3
	v_add_f32_e32 v2, v74, v75
	v_mov_b32_e32 v74, v108
	v_mov_b32_e32 v75, v92
	v_pk_mul_f32 v[74:75], v[74:75], v[10:11]
	v_pk_mul_f32 v[88:89], v[140:141], v[86:87]
	v_add_f32_e32 v6, v74, v75
	v_mov_b32_e32 v74, v76
	v_mov_b32_e32 v75, v44
	v_pk_mul_f32 v[74:75], v[74:75], v[10:11]
	v_mov_b32_e32 v44, v77
	v_add_f32_e32 v27, v74, v75
	v_mov_b32_e32 v74, v60
	v_mov_b32_e32 v75, v28
	v_pk_mul_f32 v[10:11], v[74:75], v[10:11]
	v_pk_mul_f32 v[44:45], v[44:45], v[86:87]
	v_add_f32_e32 v10, v10, v11
	v_add_f32_e32 v11, v44, v45
	v_rcp_f32_e32 v44, v4
	v_rcp_f32_e32 v4, v8
	v_mov_b32_e32 v28, v61
	v_mov_b32_e32 v60, v126
	v_mov_b32_e32 v61, v142
	v_mul_f32_e32 v45, s0, v4
	v_pk_mul_f32 v[60:61], v[60:61], v[44:45]
	v_pk_mul_f32 v[28:29], v[28:29], v[86:87]
	v_add_f32_e32 v4, v60, v61
	v_mov_b32_e32 v60, v110
	v_mov_b32_e32 v61, v94
	v_pk_mul_f32 v[60:61], v[60:61], v[44:45]
	v_add_f32_e32 v28, v28, v29
	v_add_f32_e32 v8, v60, v61
	v_mov_b32_e32 v60, v78
	v_mov_b32_e32 v61, v46
	v_pk_mul_f32 v[60:61], v[60:61], v[44:45]
	v_mov_b32_e32 v142, v127
	v_add_f32_e32 v29, v60, v61
	v_mov_b32_e32 v60, v62
	v_mov_b32_e32 v61, v30
	v_pk_mul_f32 v[44:45], v[60:61], v[44:45]
	v_rcp_f32_e32 v60, v5
	v_rcp_f32_e32 v5, v9
	v_mov_b32_e32 v30, v63
	v_add_f32_e32 v43, v44, v45
	v_mov_b32_e32 v94, v111
	v_mul_f32_e32 v61, s0, v5
	v_pk_mul_f32 v[44:45], v[142:143], v[60:61]
	v_pk_mul_f32 v[30:31], v[30:31], v[60:61]
	v_add_f32_e32 v5, v44, v45
	v_pk_mul_f32 v[44:45], v[94:95], v[60:61]
	v_mov_b32_e32 v46, v79
	v_add_f32_e32 v30, v30, v31
	v_lshlrev_b32_e32 v31, 2, v0
	v_add_f32_e32 v9, v44, v45
	v_pk_mul_f32 v[44:45], v[46:47], v[60:61]
	v_xor_b32_e32 v79, 4, v31
	v_add_f32_e32 v44, v44, v45
	v_mov_b32_e32 v160, v146
	v_mov_b32_e32 v92, v109
	v_add_f32_e32 v3, v88, v89
	v_pk_mul_f32 v[88:89], v[92:93], v[86:87]
	v_xor_b32_e32 v86, 8, v31
	v_xor_b32_e32 v87, 16, v31
	v_add_f32_e32 v7, v88, v89
	v_xor_b32_e32 v88, 32, v31
	v_xor_b32_e32 v89, 64, v31
	v_fmac_f32_e32 v97, v65, v65
	v_fmac_f32_e32 v97, v50, v50
	v_mul_f32_e32 v81, v16, v16
	v_fmac_f32_e32 v81, v32, v32
	v_fmac_f32_e32 v81, v34, v34
	v_fmac_f32_e32 v81, v18, v18
	v_mul_f32_e32 v99, v19, v19
	v_fmac_f32_e32 v99, v35, v35
	v_fmac_f32_e32 v99, v51, v51
	v_fmac_f32_e32 v99, v52, v52
	v_mul_f32_e32 v98, v66, v66
	v_fmac_f32_e32 v98, v67, v67
	v_mov_b32_e32 v161, v113
	v_fmac_f32_e32 v98, v36, v36
	v_fmac_f32_e32 v98, v20, v20
	v_mul_f32_e32 v85, v21, v21
	v_fmac_f32_e32 v85, v37, v37
	v_fmac_f32_e32 v85, v53, v53
	v_fmac_f32_e32 v85, v54, v54
	v_mul_f32_e32 v84, v68, v68
	v_fmac_f32_e32 v84, v69, v69
	v_fmac_f32_e32 v84, v38, v38
	v_fmac_f32_e32 v84, v22, v22
	v_mul_f32_e32 v83, v39, v39
	v_fmac_f32_e32 v83, v70, v70
	v_fmac_f32_e32 v83, v72, v72
	v_fmac_f32_e32 v83, v80, v80
	v_mul_f32_e32 v82, v55, v55
	v_fmac_f32_e32 v82, v56, v56
	v_fmac_f32_e32 v82, v41, v41
	v_fmac_f32_e32 v82, v57, v57
	v_mul_f32_e32 v73, v23, v23
	v_fmac_f32_e32 v73, v25, v25
	v_mov_b32_e32 v162, v97
	v_fmac_f32_e32 v73, v71, v71
	v_fmac_f32_e32 v73, v58, v58
	v_mul_f32_e32 v59, v24, v24
	v_fmac_f32_e32 v59, v40, v40
	v_fmac_f32_e32 v59, v42, v42
	v_fmac_f32_e32 v59, v26, v26
	v_mul_f32_e32 v74, v2, v2
	v_fmac_f32_e32 v74, v6, v6
	v_fmac_f32_e32 v74, v27, v27
	v_fmac_f32_e32 v74, v10, v10
	v_mul_f32_e32 v75, v3, v3
	v_fmac_f32_e32 v75, v7, v7
	v_fmac_f32_e32 v75, v11, v11
	v_fmac_f32_e32 v75, v28, v28
	v_mul_f32_e32 v76, v4, v4
	v_fmac_f32_e32 v76, v8, v8
	v_fmac_f32_e32 v76, v29, v29
	v_fmac_f32_e32 v76, v43, v43
	v_mul_f32_e32 v77, v5, v5
	v_fmac_f32_e32 v77, v9, v9
	v_mov_b32_e32 v163, v81
	v_fmac_f32_e32 v77, v44, v44
	v_fmac_f32_e32 v77, v30, v30
	v_mov_b32_e32 v90, v1
	v_mov_b32_e32 v91, v1
	s_lshl_b32 s0, s89, 13
	s_add_i32 s7, s0, 0
	v_lshlrev_b32_e32 v14, 10, v14
	s_lshl_b64 s[0:1], s[38:39], 11
	s_add_u32 s0, s46, s0
	s_addc_u32 s1, s47, s1
	v_mov_b32_e32 v164, v99
	s_lshl_b32 s6, s3, 1
	s_add_u32 s0, s0, s6
	s_addc_u32 s1, s1, 0
	v_mov_b32_e32 v165, v98
	v_mov_b32_e32 v166, v85
	v_and_b32_e32 v85, 1, v0
	v_cmp_eq_u32_e32 vcc, 0, v85
	s_nop 1
	v_mov_b32_e32 v167, v84
	v_lshlrev_b32_e32 v84, 2, v13
	v_lshlrev_b32_e32 v13, 1, v13
	v_and_b32_e32 v13, 60, v13
	v_lshl_or_b32 v13, v85, 6, v13
	v_add3_u32 v13, s7, v14, v13
	v_mov_b32_e32 v168, v83
	v_mov_b32_e32 v169, v82
	v_mov_b32_e32 v170, v73
	v_mov_b32_e32 v171, v59
	v_mov_b32_e32 v172, v74
	v_mov_b32_e32 v173, v75
	v_mov_b32_e32 v174, v76
	v_mov_b32_e32 v175, v77
	s_nop 0
	ds_bpermute_b32 v176, v79, v160
	ds_bpermute_b32 v177, v79, v161
	ds_bpermute_b32 v178, v79, v162
	ds_bpermute_b32 v179, v79, v163
	ds_bpermute_b32 v180, v79, v164
	ds_bpermute_b32 v181, v79, v165
	ds_bpermute_b32 v182, v79, v166
	ds_bpermute_b32 v183, v79, v167
	ds_bpermute_b32 v194, v79, v168
	ds_bpermute_b32 v195, v79, v169
	ds_bpermute_b32 v196, v79, v170
	ds_bpermute_b32 v197, v79, v171
	ds_bpermute_b32 v198, v79, v172
	ds_bpermute_b32 v199, v79, v173
	ds_bpermute_b32 v200, v79, v174
	ds_bpermute_b32 v201, v79, v175
	s_waitcnt lgkmcnt(0)
	v_add_f32_e32 v160, v160, v176
	v_add_f32_e32 v161, v161, v177
	v_add_f32_e32 v162, v162, v178
	v_add_f32_e32 v163, v163, v179
	v_add_f32_e32 v164, v164, v180
	v_add_f32_e32 v165, v165, v181
	v_add_f32_e32 v166, v166, v182
	v_add_f32_e32 v167, v167, v183
	v_add_f32_e32 v168, v168, v194
	v_add_f32_e32 v169, v169, v195
	v_add_f32_e32 v170, v170, v196
	v_add_f32_e32 v171, v171, v197
	v_add_f32_e32 v172, v172, v198
	v_add_f32_e32 v173, v173, v199
	v_add_f32_e32 v174, v174, v200
	v_add_f32_e32 v175, v175, v201
	ds_bpermute_b32 v176, v86, v160
	ds_bpermute_b32 v177, v86, v161
	ds_bpermute_b32 v178, v86, v162
	ds_bpermute_b32 v179, v86, v163
	ds_bpermute_b32 v180, v86, v164
	ds_bpermute_b32 v181, v86, v165
	ds_bpermute_b32 v182, v86, v166
	ds_bpermute_b32 v183, v86, v167
	ds_bpermute_b32 v194, v86, v168
	ds_bpermute_b32 v195, v86, v169
	ds_bpermute_b32 v196, v86, v170
	ds_bpermute_b32 v197, v86, v171
	ds_bpermute_b32 v198, v86, v172
	ds_bpermute_b32 v199, v86, v173
	ds_bpermute_b32 v200, v86, v174
	ds_bpermute_b32 v201, v86, v175
	s_waitcnt lgkmcnt(0)
	v_add_f32_e32 v160, v160, v176
	v_add_f32_e32 v161, v161, v177
	v_add_f32_e32 v162, v162, v178
	v_add_f32_e32 v163, v163, v179
	v_add_f32_e32 v164, v164, v180
	v_add_f32_e32 v165, v165, v181
	v_add_f32_e32 v166, v166, v182
	v_add_f32_e32 v167, v167, v183
	v_add_f32_e32 v168, v168, v194
	v_add_f32_e32 v169, v169, v195
	v_add_f32_e32 v170, v170, v196
	v_add_f32_e32 v171, v171, v197
	v_add_f32_e32 v172, v172, v198
	v_add_f32_e32 v173, v173, v199
	v_add_f32_e32 v174, v174, v200
	v_add_f32_e32 v175, v175, v201
	ds_bpermute_b32 v176, v87, v160
	ds_bpermute_b32 v177, v87, v161
	ds_bpermute_b32 v178, v87, v162
	ds_bpermute_b32 v179, v87, v163
	ds_bpermute_b32 v180, v87, v164
	ds_bpermute_b32 v181, v87, v165
	ds_bpermute_b32 v182, v87, v166
	ds_bpermute_b32 v183, v87, v167
	ds_bpermute_b32 v194, v87, v168
	ds_bpermute_b32 v195, v87, v169
	ds_bpermute_b32 v196, v87, v170
	ds_bpermute_b32 v197, v87, v171
	ds_bpermute_b32 v198, v87, v172
	ds_bpermute_b32 v199, v87, v173
	ds_bpermute_b32 v200, v87, v174
	ds_bpermute_b32 v201, v87, v175
	s_waitcnt lgkmcnt(0)
	v_add_f32_e32 v160, v160, v176
	v_add_f32_e32 v161, v161, v177
	v_add_f32_e32 v162, v162, v178
	v_add_f32_e32 v163, v163, v179
	v_add_f32_e32 v164, v164, v180
	v_add_f32_e32 v165, v165, v181
	v_add_f32_e32 v166, v166, v182
	v_add_f32_e32 v167, v167, v183
	v_add_f32_e32 v168, v168, v194
	v_add_f32_e32 v169, v169, v195
	v_add_f32_e32 v170, v170, v196
	v_add_f32_e32 v171, v171, v197
	v_add_f32_e32 v172, v172, v198
	v_add_f32_e32 v173, v173, v199
	v_add_f32_e32 v174, v174, v200
	v_add_f32_e32 v175, v175, v201
	ds_bpermute_b32 v176, v88, v160
	ds_bpermute_b32 v177, v88, v161
	ds_bpermute_b32 v178, v88, v162
	ds_bpermute_b32 v179, v88, v163
	ds_bpermute_b32 v180, v88, v164
	ds_bpermute_b32 v181, v88, v165
	ds_bpermute_b32 v182, v88, v166
	ds_bpermute_b32 v183, v88, v167
	ds_bpermute_b32 v194, v88, v168
	ds_bpermute_b32 v195, v88, v169
	ds_bpermute_b32 v196, v88, v170
	ds_bpermute_b32 v197, v88, v171
	ds_bpermute_b32 v198, v88, v172
	ds_bpermute_b32 v199, v88, v173
	ds_bpermute_b32 v200, v88, v174
	ds_bpermute_b32 v201, v88, v175
	s_waitcnt lgkmcnt(0)
	v_add_f32_e32 v160, v160, v176
	v_add_f32_e32 v161, v161, v177
	v_add_f32_e32 v162, v162, v178
	v_add_f32_e32 v163, v163, v179
	v_add_f32_e32 v164, v164, v180
	v_add_f32_e32 v165, v165, v181
	v_add_f32_e32 v166, v166, v182
	v_add_f32_e32 v167, v167, v183
	v_add_f32_e32 v168, v168, v194
	v_add_f32_e32 v169, v169, v195
	v_add_f32_e32 v170, v170, v196
	v_add_f32_e32 v171, v171, v197
	v_add_f32_e32 v172, v172, v198
	v_add_f32_e32 v173, v173, v199
	v_add_f32_e32 v174, v174, v200
	v_add_f32_e32 v175, v175, v201
	ds_bpermute_b32 v176, v89, v160
	ds_bpermute_b32 v177, v89, v161
	ds_bpermute_b32 v178, v89, v162
	ds_bpermute_b32 v179, v89, v163
	ds_bpermute_b32 v180, v89, v164
	ds_bpermute_b32 v181, v89, v165
	ds_bpermute_b32 v182, v89, v166
	ds_bpermute_b32 v183, v89, v167
	ds_bpermute_b32 v194, v89, v168
	ds_bpermute_b32 v195, v89, v169
	ds_bpermute_b32 v196, v89, v170
	ds_bpermute_b32 v197, v89, v171
	ds_bpermute_b32 v198, v89, v172
	ds_bpermute_b32 v199, v89, v173
	ds_bpermute_b32 v200, v89, v174
	ds_bpermute_b32 v201, v89, v175
	s_waitcnt lgkmcnt(0)
	v_add_f32_e32 v160, v160, v176
	v_add_f32_e32 v161, v161, v177
	v_add_f32_e32 v162, v162, v178
	v_add_f32_e32 v163, v163, v179
	v_add_f32_e32 v164, v164, v180
	v_add_f32_e32 v165, v165, v181
	v_add_f32_e32 v166, v166, v182
	v_add_f32_e32 v167, v167, v183
	v_add_f32_e32 v168, v168, v194
	v_add_f32_e32 v169, v169, v195
	v_add_f32_e32 v170, v170, v196
	v_add_f32_e32 v171, v171, v197
	v_add_f32_e32 v172, v172, v198
	v_add_f32_e32 v173, v173, v199
	v_add_f32_e32 v174, v174, v200
	v_add_f32_e32 v175, v175, v201
	v_mov_b32_e32 v31, v160
	v_mov_b32_e32 v45, v161
	v_mov_b32_e32 v46, v162
	v_fmamk_f32 v31, v31, 0x3c000000, v222
	v_rsq_f32_e32 v31, v31
	s_nop 0
	v_fmamk_f32 v45, v45, 0x3c000000, v222
	v_mul_f32_e32 v31, 0x3f4ccccd, v31
	v_rsq_f32_e32 v45, v45
	s_nop 0
	v_mul_f32_e32 v45, 0x3f4ccccd, v45
	v_fmamk_f32 v46, v46, 0x3c000000, v222
	v_mul_f32_e32 v33, v33, v45
	v_rsq_f32_e32 v46, v46
	s_nop 0
	v_mul_f32_e32 v46, 0x3f4ccccd, v46
	v_mov_b32_e32 v47, v163
	v_fmamk_f32 v47, v47, 0x3c000000, v222
	v_rsq_f32_e32 v47, v47
	s_nop 0
	v_mul_f32_e32 v47, 0x3f4ccccd, v47
	v_mov_b32_e32 v60, v164
	v_fmamk_f32 v60, v60, 0x3c000000, v222
	v_rsq_f32_e32 v60, v60
	s_nop 0
	v_mul_f32_e32 v60, 0x3f4ccccd, v60
	v_mov_b32_e32 v61, v165
	v_fmamk_f32 v61, v61, 0x3c000000, v222
	v_rsq_f32_e32 v61, v61
	s_nop 0
	v_mul_f32_e32 v61, 0x3f4ccccd, v61
	v_mov_b32_e32 v62, v166
	v_fmamk_f32 v62, v62, 0x3c000000, v222
	v_rsq_f32_e32 v62, v62
	s_nop 0
	v_mul_f32_e32 v14, v48, v45
	v_mul_f32_e32 v62, 0x3f4ccccd, v62
	v_mov_b32_e32 v63, v167
	v_fmamk_f32 v63, v63, 0x3c000000, v222
	v_rsq_f32_e32 v63, v63
	s_nop 0
	v_mul_f32_e32 v63, 0x3f4ccccd, v63
	v_mov_b32_e32 v78, v168
	v_fmamk_f32 v78, v78, 0x3c000000, v222
	v_rsq_f32_e32 v78, v78
	s_nop 0
	v_mul_f32_e32 v78, 0x3f4ccccd, v78
	v_mov_b32_e32 v81, v169
	v_fmamk_f32 v81, v81, 0x3c000000, v222
	v_rsq_f32_e32 v81, v81
	s_nop 0
	v_mul_f32_e32 v81, 0x3f4ccccd, v81
	v_mov_b32_e32 v73, v170
	v_fmamk_f32 v73, v73, 0x3c000000, v222
	v_rsq_f32_e32 v73, v73
	s_nop 0
	v_mul_f32_e32 v73, 0x3f4ccccd, v73
	v_mov_b32_e32 v59, v171
	v_fmamk_f32 v59, v59, 0x3c000000, v222
	v_rsq_f32_e32 v59, v59
	s_nop 0
	v_mul_f32_e32 v83, 0x3f4ccccd, v59
	v_mov_b32_e32 v59, v172
	v_fmamk_f32 v59, v59, 0x3c000000, v222
	v_rsq_f32_e32 v59, v59
	s_nop 0
	v_mul_f32_e32 v82, 0x3f4ccccd, v59
	v_mul_f32_e32 v2, v2, v82
	v_mul_f32_e32 v6, v6, v82
	v_mul_f32_e32 v10, v10, v82
	v_mov_b32_e32 v59, v173
	v_fmamk_f32 v59, v59, 0x3c000000, v222
	v_rsq_f32_e32 v59, v59
	s_nop 0
	v_mul_f32_e32 v75, 0x3f4ccccd, v59
	v_mov_b32_e32 v59, v174
	v_fmamk_f32 v59, v59, 0x3c000000, v222
	v_rsq_f32_e32 v59, v59
	s_nop 0
	v_mul_f32_e32 v74, 0x3f4ccccd, v59
	v_mul_f32_e32 v86, v112, v31
	v_mul_f32_e32 v87, v96, v31
	v_mul_f32_e32 v88, v144, v31
	v_mul_f32_e32 v31, v145, v31
	v_mov_b32_e32 v59, v175
	global_load_dword v76, v84, s[22:23]
	global_load_dword v77, v84, s[22:23] offset:128
	global_load_dword v79, v84, s[22:23] offset:256
	s_nop 0
	global_load_dword v84, v84, s[22:23] offset:384
	v_fmamk_f32 v59, v59, 0x3c000000, v222
	v_rsq_f32_e32 v59, v59
	s_waitcnt vmcnt(0)
	v_mul_f32_e32 v86, v86, v76
	v_mul_f32_e32 v87, v87, v77
	v_mul_f32_e32 v88, v88, v79
	v_mul_f32_e32 v31, v31, v84
	v_cndmask_b32_e32 v89, v86, v87, vcc
	v_mul_f32_e32 v14, v14, v76
	v_mul_f32_e32 v33, v33, v79
	v_mov_b32_dpp v90, v89 quad_perm:[1,0,3,2] row_mask:0xf bank_mask:0xf
	v_cndmask_b32_e32 v89, v88, v31, vcc
	v_cndmask_b32_e32 v87, v87, v90, vcc
	v_cndmask_b32_e32 v86, v90, v86, vcc
	v_mov_b32_dpp v91, v89 quad_perm:[1,0,3,2] row_mask:0xf bank_mask:0xf
	v_cvt_pk_bf16_f32 v86, v86, v87
	v_cndmask_b32_e32 v31, v31, v91, vcc
	v_cndmask_b32_e32 v87, v91, v88, vcc
	v_cvt_pk_bf16_f32 v31, v87, v31
	ds_write2_b32 v13, v86, v31 offset1:32
	v_mul_f32_e32 v31, v64, v45
	v_mul_f32_e32 v31, v31, v77
	v_mul_f32_e32 v45, v49, v45
	v_mul_f32_e32 v45, v45, v84
	v_cndmask_b32_e32 v48, v14, v31, vcc
	v_mov_b32_e32 v49, v1
	v_mov_b32_e32 v64, v1
	v_mul_f32_e32 v2, v2, v76
	v_mov_b32_dpp v49, v48 quad_perm:[1,0,3,2] row_mask:0xf bank_mask:0xf
	v_cndmask_b32_e32 v48, v33, v45, vcc
	v_cndmask_b32_e32 v31, v31, v49, vcc
	v_cndmask_b32_e32 v14, v49, v14, vcc
	v_mov_b32_dpp v64, v48 quad_perm:[1,0,3,2] row_mask:0xf bank_mask:0xf
	v_cvt_pk_bf16_f32 v14, v14, v31
	v_cndmask_b32_e32 v31, v45, v64, vcc
	v_cndmask_b32_e32 v33, v64, v33, vcc
	v_cvt_pk_bf16_f32 v31, v33, v31
	ds_write2_b32 v13, v14, v31 offset0:64 offset1:96
	v_mul_f32_e32 v14, v15, v46
	v_mul_f32_e32 v15, v17, v46
	v_mul_f32_e32 v14, v14, v76
	v_mul_f32_e32 v15, v15, v77
	v_mul_f32_e32 v17, v65, v46
	v_mul_f32_e32 v31, v50, v46
	v_mul_f32_e32 v17, v17, v79
	v_mul_f32_e32 v31, v31, v84
	v_cndmask_b32_e32 v33, v14, v15, vcc
	v_mov_b32_e32 v45, v1
	v_mov_b32_e32 v46, v1
	v_mul_f32_e32 v6, v6, v77
	v_mov_b32_dpp v45, v33 quad_perm:[1,0,3,2] row_mask:0xf bank_mask:0xf
	v_cndmask_b32_e32 v33, v17, v31, vcc
	v_cndmask_b32_e32 v15, v15, v45, vcc
	v_cndmask_b32_e32 v14, v45, v14, vcc
	v_mov_b32_dpp v46, v33 quad_perm:[1,0,3,2] row_mask:0xf bank_mask:0xf
	v_cvt_pk_bf16_f32 v14, v14, v15
	v_cndmask_b32_e32 v15, v31, v46, vcc
	v_cndmask_b32_e32 v17, v46, v17, vcc
	v_cvt_pk_bf16_f32 v15, v17, v15
	ds_write2_b32 v13, v14, v15 offset0:128 offset1:160
	v_mul_f32_e32 v14, v16, v47
	v_mul_f32_e32 v15, v32, v47
	v_mul_f32_e32 v14, v14, v76
	v_mul_f32_e32 v15, v15, v77
	v_mul_f32_e32 v16, v34, v47
	v_mul_f32_e32 v17, v18, v47
	v_mul_f32_e32 v16, v16, v79
	v_mul_f32_e32 v17, v17, v84
	v_cndmask_b32_e32 v18, v14, v15, vcc
	v_mov_b32_e32 v31, v1
	v_mov_b32_e32 v32, v1
	v_mul_f32_e32 v10, v10, v84
	v_mov_b32_dpp v31, v18 quad_perm:[1,0,3,2] row_mask:0xf bank_mask:0xf
	v_cndmask_b32_e32 v18, v16, v17, vcc
	v_cndmask_b32_e32 v15, v15, v31, vcc
	v_cndmask_b32_e32 v14, v31, v14, vcc
	v_mov_b32_dpp v32, v18 quad_perm:[1,0,3,2] row_mask:0xf bank_mask:0xf
	v_cvt_pk_bf16_f32 v14, v14, v15
	v_cndmask_b32_e32 v15, v17, v32, vcc
	v_cndmask_b32_e32 v16, v32, v16, vcc
	v_cvt_pk_bf16_f32 v15, v16, v15
	ds_write2_b32 v13, v14, v15 offset0:192 offset1:224
	v_mul_f32_e32 v14, v19, v60
	v_mul_f32_e32 v15, v35, v60
	v_mul_f32_e32 v14, v14, v76
	v_mul_f32_e32 v15, v15, v77
	v_mul_f32_e32 v16, v51, v60
	v_mul_f32_e32 v17, v52, v60
	v_mul_f32_e32 v16, v16, v79
	v_mul_f32_e32 v17, v17, v84
	v_cndmask_b32_e32 v18, v14, v15, vcc
	v_mov_b32_e32 v19, v1
	v_mov_b32_e32 v31, v1
	v_mul_f32_e32 v59, 0x3f4ccccd, v59
	v_mov_b32_dpp v19, v18 quad_perm:[1,0,3,2] row_mask:0xf bank_mask:0xf
	v_cndmask_b32_e32 v18, v16, v17, vcc
	v_cndmask_b32_e32 v15, v15, v19, vcc
	v_cndmask_b32_e32 v14, v19, v14, vcc
	v_mov_b32_dpp v31, v18 quad_perm:[1,0,3,2] row_mask:0xf bank_mask:0xf
	v_cvt_pk_bf16_f32 v14, v14, v15
	v_cndmask_b32_e32 v15, v17, v31, vcc
	v_cndmask_b32_e32 v16, v31, v16, vcc
	v_cvt_pk_bf16_f32 v15, v16, v15
	v_add_u32_e32 v16, 0x800, v13
	ds_write2_b32 v16, v14, v15 offset1:32
	v_mul_f32_e32 v14, v66, v61
	v_mul_f32_e32 v15, v67, v61
	v_mul_f32_e32 v14, v14, v76
	v_mul_f32_e32 v15, v15, v77
	v_mul_f32_e32 v17, v36, v61
	v_mul_f32_e32 v18, v20, v61
	v_mul_f32_e32 v17, v17, v79
	v_mul_f32_e32 v18, v18, v84
	v_cndmask_b32_e32 v19, v14, v15, vcc
	v_mov_b32_e32 v20, v1
	v_mov_b32_e32 v31, v1
	s_nop 0
	v_mov_b32_dpp v20, v19 quad_perm:[1,0,3,2] row_mask:0xf bank_mask:0xf
	v_cndmask_b32_e32 v19, v17, v18, vcc
	v_cndmask_b32_e32 v15, v15, v20, vcc
	v_cndmask_b32_e32 v14, v20, v14, vcc
	v_mov_b32_dpp v31, v19 quad_perm:[1,0,3,2] row_mask:0xf bank_mask:0xf
	v_cvt_pk_bf16_f32 v14, v14, v15
	v_cndmask_b32_e32 v15, v18, v31, vcc
	v_cndmask_b32_e32 v17, v31, v17, vcc
	v_cvt_pk_bf16_f32 v15, v17, v15
	ds_write2_b32 v16, v14, v15 offset0:64 offset1:96
	v_mul_f32_e32 v14, v21, v62
	v_mul_f32_e32 v15, v37, v62
	v_mul_f32_e32 v14, v14, v76
	v_mul_f32_e32 v15, v15, v77
	v_mul_f32_e32 v17, v53, v62
	v_mul_f32_e32 v18, v54, v62
	v_mul_f32_e32 v17, v17, v79
	v_mul_f32_e32 v18, v18, v84
	v_cndmask_b32_e32 v19, v14, v15, vcc
	v_mov_b32_e32 v20, v1
	v_mov_b32_e32 v21, v1
	s_nop 0
	v_mov_b32_dpp v20, v19 quad_perm:[1,0,3,2] row_mask:0xf bank_mask:0xf
	v_cndmask_b32_e32 v19, v17, v18, vcc
	v_cndmask_b32_e32 v15, v15, v20, vcc
	v_cndmask_b32_e32 v14, v20, v14, vcc
	v_mov_b32_dpp v21, v19 quad_perm:[1,0,3,2] row_mask:0xf bank_mask:0xf
	v_cvt_pk_bf16_f32 v14, v14, v15
	v_cndmask_b32_e32 v15, v18, v21, vcc
	v_cndmask_b32_e32 v17, v21, v17, vcc
	v_cvt_pk_bf16_f32 v15, v17, v15
	ds_write2_b32 v16, v14, v15 offset0:128 offset1:160
	v_mul_f32_e32 v14, v68, v63
	v_mul_f32_e32 v15, v69, v63
	v_mul_f32_e32 v14, v14, v76
	v_mul_f32_e32 v15, v15, v77
	v_mul_f32_e32 v17, v38, v63
	v_mul_f32_e32 v18, v22, v63
	v_mul_f32_e32 v17, v17, v79
	v_mul_f32_e32 v18, v18, v84
	v_cndmask_b32_e32 v19, v14, v15, vcc
	v_mov_b32_e32 v20, v1
	v_mov_b32_e32 v21, v1
	s_nop 0
	v_mov_b32_dpp v20, v19 quad_perm:[1,0,3,2] row_mask:0xf bank_mask:0xf
	v_cndmask_b32_e32 v19, v17, v18, vcc
	v_cndmask_b32_e32 v15, v15, v20, vcc
	v_cndmask_b32_e32 v14, v20, v14, vcc
	v_mov_b32_dpp v21, v19 quad_perm:[1,0,3,2] row_mask:0xf bank_mask:0xf
	v_cvt_pk_bf16_f32 v14, v14, v15
	v_cndmask_b32_e32 v15, v18, v21, vcc
	v_cndmask_b32_e32 v17, v21, v17, vcc
	v_cvt_pk_bf16_f32 v15, v17, v15
	ds_write2_b32 v16, v14, v15 offset0:192 offset1:224
	v_mul_f32_e32 v14, v39, v78
	v_mul_f32_e32 v15, v70, v78
	v_mul_f32_e32 v14, v14, v76
	v_mul_f32_e32 v15, v15, v77
	v_mul_f32_e32 v16, v72, v78
	v_mul_f32_e32 v17, v80, v78
	v_mul_f32_e32 v16, v16, v79
	v_mul_f32_e32 v17, v17, v84
	v_cndmask_b32_e32 v18, v14, v15, vcc
	v_mov_b32_e32 v19, v1
	v_mov_b32_e32 v20, v1
	v_mov_b32_e32 v21, v1
	v_mov_b32_dpp v19, v18 quad_perm:[1,0,3,2] row_mask:0xf bank_mask:0xf
	v_cndmask_b32_e32 v18, v16, v17, vcc
	v_cndmask_b32_e32 v15, v15, v19, vcc
	v_cndmask_b32_e32 v14, v19, v14, vcc
	v_mov_b32_dpp v20, v18 quad_perm:[1,0,3,2] row_mask:0xf bank_mask:0xf
	v_cvt_pk_bf16_f32 v14, v14, v15
	v_cndmask_b32_e32 v15, v17, v20, vcc
	v_cndmask_b32_e32 v16, v20, v16, vcc
	v_cvt_pk_bf16_f32 v15, v16, v15
	v_add_u32_e32 v16, 0x1000, v13
	ds_write2_b32 v16, v14, v15 offset1:32
	v_mul_f32_e32 v14, v55, v81
	v_mul_f32_e32 v15, v56, v81
	v_mul_f32_e32 v14, v14, v76
	v_mul_f32_e32 v15, v15, v77
	v_mul_f32_e32 v17, v41, v81
	v_mul_f32_e32 v18, v57, v81
	v_mul_f32_e32 v17, v17, v79
	v_mul_f32_e32 v18, v18, v84
	v_cndmask_b32_e32 v19, v14, v15, vcc
	v_mov_b32_e32 v20, v1
	s_nop 1
	v_mov_b32_dpp v20, v19 quad_perm:[1,0,3,2] row_mask:0xf bank_mask:0xf
	v_cndmask_b32_e32 v19, v17, v18, vcc
	v_cndmask_b32_e32 v15, v15, v20, vcc
	v_cndmask_b32_e32 v14, v20, v14, vcc
	v_mov_b32_dpp v21, v19 quad_perm:[1,0,3,2] row_mask:0xf bank_mask:0xf
	v_cvt_pk_bf16_f32 v14, v14, v15
	v_cndmask_b32_e32 v15, v18, v21, vcc
	v_cndmask_b32_e32 v17, v21, v17, vcc
	v_cvt_pk_bf16_f32 v15, v17, v15
	ds_write2_b32 v16, v14, v15 offset0:64 offset1:96
	v_mul_f32_e32 v14, v23, v73
	v_mul_f32_e32 v15, v25, v73
	v_mul_f32_e32 v14, v14, v76
	v_mul_f32_e32 v15, v15, v77
	v_mul_f32_e32 v17, v71, v73
	v_mul_f32_e32 v18, v58, v73
	v_mul_f32_e32 v17, v17, v79
	v_mul_f32_e32 v18, v18, v84
	v_cndmask_b32_e32 v19, v14, v15, vcc
	v_mov_b32_e32 v20, v1
	v_mov_b32_e32 v21, v1
	s_nop 0
	v_mov_b32_dpp v20, v19 quad_perm:[1,0,3,2] row_mask:0xf bank_mask:0xf
	v_cndmask_b32_e32 v19, v17, v18, vcc
	v_cndmask_b32_e32 v15, v15, v20, vcc
	v_cndmask_b32_e32 v14, v20, v14, vcc
	v_mov_b32_dpp v21, v19 quad_perm:[1,0,3,2] row_mask:0xf bank_mask:0xf
	v_cvt_pk_bf16_f32 v14, v14, v15
	v_cndmask_b32_e32 v15, v18, v21, vcc
	v_cndmask_b32_e32 v17, v21, v17, vcc
	v_cvt_pk_bf16_f32 v15, v17, v15
	ds_write2_b32 v16, v14, v15 offset0:128 offset1:160
	v_mul_f32_e32 v14, v24, v83
	v_mul_f32_e32 v15, v40, v83
	v_mul_f32_e32 v14, v14, v76
	v_mul_f32_e32 v15, v15, v77
	v_mul_f32_e32 v17, v42, v83
	v_mul_f32_e32 v18, v26, v83
	v_mul_f32_e32 v17, v17, v79
	v_mul_f32_e32 v18, v18, v84
	v_cndmask_b32_e32 v19, v14, v15, vcc
	v_mov_b32_e32 v20, v1
	v_mov_b32_e32 v21, v1
	s_nop 0
	v_mov_b32_dpp v20, v19 quad_perm:[1,0,3,2] row_mask:0xf bank_mask:0xf
	v_cndmask_b32_e32 v19, v17, v18, vcc
	v_cndmask_b32_e32 v15, v15, v20, vcc
	v_cndmask_b32_e32 v14, v20, v14, vcc
	v_mov_b32_dpp v21, v19 quad_perm:[1,0,3,2] row_mask:0xf bank_mask:0xf
	v_cvt_pk_bf16_f32 v14, v14, v15
	v_cndmask_b32_e32 v15, v18, v21, vcc
	v_cndmask_b32_e32 v17, v21, v17, vcc
	v_cvt_pk_bf16_f32 v15, v17, v15
	ds_write2_b32 v16, v14, v15 offset0:192 offset1:224
	v_mul_f32_e32 v14, v27, v82
	v_mul_f32_e32 v14, v14, v79
	v_cndmask_b32_e32 v15, v2, v6, vcc
	v_mov_b32_e32 v16, v1
	v_mov_b32_e32 v17, v1
	s_nop 0
	v_mov_b32_dpp v16, v15 quad_perm:[1,0,3,2] row_mask:0xf bank_mask:0xf
	v_cndmask_b32_e32 v15, v14, v10, vcc
	v_cndmask_b32_e32 v6, v6, v16, vcc
	v_cndmask_b32_e32 v2, v16, v2, vcc
	v_mov_b32_dpp v17, v15 quad_perm:[1,0,3,2] row_mask:0xf bank_mask:0xf
	v_cvt_pk_bf16_f32 v2, v2, v6
	v_cndmask_b32_e32 v6, v10, v17, vcc
	v_cndmask_b32_e32 v10, v17, v14, vcc
	v_cvt_pk_bf16_f32 v6, v10, v6
	v_add_u32_e32 v10, 0x1800, v13
	ds_write2_b32 v10, v2, v6 offset1:32
	v_mul_f32_e32 v2, v3, v75
	v_mul_f32_e32 v3, v7, v75
	v_mul_f32_e32 v2, v2, v76
	v_mul_f32_e32 v3, v3, v77
	v_mul_f32_e32 v6, v11, v75
	v_mul_f32_e32 v7, v28, v75
	v_mul_f32_e32 v6, v6, v79
	v_mul_f32_e32 v7, v7, v84
	v_cndmask_b32_e32 v11, v2, v3, vcc
	v_mov_b32_e32 v13, v1
	v_mov_b32_e32 v14, v1
	s_nop 0
	v_mov_b32_dpp v13, v11 quad_perm:[1,0,3,2] row_mask:0xf bank_mask:0xf
	v_cndmask_b32_e32 v11, v6, v7, vcc
	v_cndmask_b32_e32 v3, v3, v13, vcc
	v_cndmask_b32_e32 v2, v13, v2, vcc
	v_mov_b32_dpp v14, v11 quad_perm:[1,0,3,2] row_mask:0xf bank_mask:0xf
	v_cvt_pk_bf16_f32 v2, v2, v3
	v_cndmask_b32_e32 v3, v7, v14, vcc
	v_cndmask_b32_e32 v6, v14, v6, vcc
	v_cvt_pk_bf16_f32 v3, v6, v3
	ds_write2_b32 v10, v2, v3 offset0:64 offset1:96
	v_mul_f32_e32 v2, v4, v74
	v_mul_f32_e32 v3, v8, v74
	v_mul_f32_e32 v2, v76, v2
	v_mul_f32_e32 v3, v77, v3
	v_mul_f32_e32 v4, v29, v74
	v_mul_f32_e32 v6, v43, v74
	v_mul_f32_e32 v4, v4, v79
	v_mul_f32_e32 v6, v6, v84
	v_cndmask_b32_e32 v7, v2, v3, vcc
	v_mov_b32_e32 v8, v1
	v_mov_b32_e32 v11, v1
	s_nop 0
	v_mov_b32_dpp v8, v7 quad_perm:[1,0,3,2] row_mask:0xf bank_mask:0xf
	v_cndmask_b32_e32 v7, v4, v6, vcc
	v_cndmask_b32_e32 v3, v3, v8, vcc
	v_cndmask_b32_e32 v2, v8, v2, vcc
	v_mov_b32_dpp v11, v7 quad_perm:[1,0,3,2] row_mask:0xf bank_mask:0xf
	v_cvt_pk_bf16_f32 v2, v2, v3
	v_cndmask_b32_e32 v3, v6, v11, vcc
	v_cndmask_b32_e32 v4, v11, v4, vcc
	v_cvt_pk_bf16_f32 v3, v4, v3
	ds_write2_b32 v10, v2, v3 offset0:128 offset1:160
	v_mul_f32_e32 v2, v5, v59
	v_mul_f32_e32 v3, v9, v59
	v_mul_f32_e32 v2, v76, v2
	v_mul_f32_e32 v3, v77, v3
	v_mul_f32_e32 v4, v44, v59
	v_mul_f32_e32 v5, v30, v59
	v_mul_f32_e32 v4, v79, v4
	v_mul_f32_e32 v5, v84, v5
	v_cndmask_b32_e32 v6, v2, v3, vcc
	v_mov_b32_e32 v7, v1
	v_mov_b32_e32 v8, v1
	s_nop 0
	v_mov_b32_dpp v7, v6 quad_perm:[1,0,3,2] row_mask:0xf bank_mask:0xf
	v_cndmask_b32_e32 v6, v4, v5, vcc
	v_cndmask_b32_e32 v3, v3, v7, vcc
	v_cndmask_b32_e32 v2, v7, v2, vcc
	v_mov_b32_dpp v8, v6 quad_perm:[1,0,3,2] row_mask:0xf bank_mask:0xf
	v_cvt_pk_bf16_f32 v2, v2, v3
	v_cndmask_b32_e32 v3, v5, v8, vcc
	v_cndmask_b32_e32 v4, v8, v4, vcc
	v_cvt_pk_bf16_f32 v3, v4, v3
	v_ashrrev_i32_e32 v8, 4, v0
	v_and_b32_e32 v0, 15, v0
	ds_write2_b32 v10, v2, v3 offset0:192 offset1:224
	v_lshl_add_u32 v9, v0, 4, s7
	s_waitcnt lgkmcnt(0)
	v_lshlrev_b32_e32 v10, 3, v0
	v_lshl_add_u32 v0, v8, 8, v9
	ds_read_b128 v[2:5], v0
	v_lshl_or_b32 v0, v8, 10, v10
	v_lshl_add_u64 v[6:7], v[0:1], 1, s[0:1]
	v_add_u32_e32 v0, 4, v8
	v_cmp_eq_u32_e32 vcc, 0, v12
	s_waitcnt lgkmcnt(0)
	global_store_dwordx4 v[6:7], v[2:5], off
	s_and_b64 vcc, exec, vcc
	s_nop 0
	v_lshl_add_u32 v2, v0, 8, v9
	ds_read_b128 v[2:5], v2
	v_lshl_or_b32 v0, v0, 10, v10
	v_lshl_add_u64 v[6:7], v[0:1], 1, s[0:1]
	v_add_u32_e32 v0, 8, v8
	s_waitcnt lgkmcnt(0)
	global_store_dwordx4 v[6:7], v[2:5], off
	s_nop 1
	v_lshl_add_u32 v2, v0, 8, v9
	ds_read_b128 v[2:5], v2
	v_lshl_or_b32 v0, v0, 10, v10
	v_lshl_add_u64 v[6:7], v[0:1], 1, s[0:1]
	v_add_u32_e32 v0, 12, v8
	s_waitcnt lgkmcnt(0)
	global_store_dwordx4 v[6:7], v[2:5], off
	s_nop 1
	v_lshl_add_u32 v2, v0, 8, v9
	ds_read_b128 v[2:5], v2
	v_lshl_or_b32 v0, v0, 10, v10
	v_lshl_add_u64 v[6:7], v[0:1], 1, s[0:1]
	v_add_u32_e32 v0, 16, v8
	s_waitcnt lgkmcnt(0)
	global_store_dwordx4 v[6:7], v[2:5], off
	s_nop 1
	v_lshl_add_u32 v2, v0, 8, v9
	ds_read_b128 v[2:5], v2
	v_lshl_or_b32 v0, v0, 10, v10
	v_lshl_add_u64 v[6:7], v[0:1], 1, s[0:1]
	v_add_u32_e32 v0, 20, v8
	s_waitcnt lgkmcnt(0)
	global_store_dwordx4 v[6:7], v[2:5], off
	s_nop 1
	v_lshl_add_u32 v2, v0, 8, v9
	ds_read_b128 v[2:5], v2
	v_lshl_or_b32 v0, v0, 10, v10
	v_lshl_add_u64 v[6:7], v[0:1], 1, s[0:1]
	v_add_u32_e32 v0, 24, v8
	s_waitcnt lgkmcnt(0)
	global_store_dwordx4 v[6:7], v[2:5], off
	s_nop 1
	v_lshl_add_u32 v2, v0, 8, v9
	ds_read_b128 v[2:5], v2
	v_lshl_or_b32 v0, v0, 10, v10
	v_lshl_add_u64 v[6:7], v[0:1], 1, s[0:1]
	v_add_u32_e32 v0, 28, v8
	s_waitcnt lgkmcnt(0)
	global_store_dwordx4 v[6:7], v[2:5], off
	s_nop 1
	v_lshl_add_u32 v2, v0, 8, v9
	ds_read_b128 v[2:5], v2
	v_lshl_or_b32 v0, v0, 10, v10
	v_lshl_add_u64 v[6:7], v[0:1], 1, s[0:1]
	s_waitcnt lgkmcnt(0)
	global_store_dwordx4 v[6:7], v[2:5], off
	s_waitcnt lgkmcnt(0)
	s_barrier
	s_cbranch_vccnz .LBB0_168
	v_mbcnt_lo_u32_b32 v0, -1, 0
	v_mbcnt_hi_u32_b32 v0, -1, v0
	s_nop 0
	v_add_u32_e32 v2, s92, v0
	s_nop 0
	v_readfirstlane_b32 s3, v2
	v_cmp_gt_i32_e32 vcc, s48, v2
	s_and_saveexec_b64 s[38:39], vcc
	s_cbranch_execz .LBB0_233
	v_max_i32_e32 v0, 0x380, v2
	v_sub_u32_e32 v0, v0, v2
	v_add_u32_e32 v0, 0x1ff, v0
	s_movk_i32 s0, 0x1ff
	v_cmp_lt_u32_e32 vcc, s0, v0
	s_mov_b64 s[0:1], -1
	v_mov_b32_e32 v3, v2
	s_and_saveexec_b64 s[40:41], vcc
	s_cbranch_execz .LBB0_230
	v_lshrrev_b32_e32 v0, 9, v0
	v_add_u32_e32 v6, 1, v0
	v_and_b32_e32 v7, 0xfffffe, v6
	v_add_u32_e32 v3, 0x200, v2
	v_readlane_b32 s0, v255, 14
	s_mov_b32 s7, s75
	s_mov_b64 s[42:43], 0
	v_lshl_add_u32 v8, v2, 2, s0
	v_mov_b32_e32 v9, v7
	v_mov_b64_e32 v[4:5], v[2:3]
